# MLA up-projection epilogue part 1: k_pe row pieces of all 8 row groups requested together in row group 0 (16 loads in flight, one wait) instead of 2 dependent loads + vmcnt(0) per row group
# speedup vs baseline: 1.0021x; 1.0021x over previous
.LBB0_400:
	s_lshl_b32 s48, s8, 8
	s_cmp_lg_u32 s58, 0
	v_mbcnt_lo_u32_b32 v112, -1, 0
	v_mbcnt_hi_u32_b32 v112, -1, v112
	s_cselect_b64 s[62:63], -1, 0
	v_and_b32_e32 v237, 15, v112
	s_cmp_eq_u32 s58, 0
	v_or_b32_e32 v231, s85, v237
	s_cselect_b32 s6, 0, 32
	v_add_u32_e32 v232, s48, v231
	s_add_u32 s16, s77, s6
	v_ashrrev_i32_e32 v233, 31, v232
	s_addc_u32 s17, s78, 0
	v_lshlrev_b64 v[114:115], 6, v[232:233]
	v_lshl_add_u64 v[118:119], s[16:17], 0, v[114:115]
	global_load_dwordx4 v[114:117], v[118:119], off
	global_load_dwordx4 v[128:131], v[118:119], off offset:16
	v_mul_f32_e32 v118, v157, v157
	v_mul_f32_e32 v119, v159, v159
	v_mul_f32_e32 v132, v153, v153
	v_mul_f32_e32 v133, v155, v155
	v_fmac_f32_e32 v118, v156, v156
	v_fmac_f32_e32 v119, v158, v158
	v_fmac_f32_e32 v132, v152, v152
	v_fmac_f32_e32 v133, v154, v154
	v_add_f32_e32 v118, v118, v119
	v_ashrrev_i32_e32 v135, 2, v112
	v_cndmask_b32_e64 v134, 0, 1, s[44:45]
	v_and_b32_e32 v208, -4, v135
	s_mov_b64 s[10:11], -1
	v_cmp_ne_u32_e64 s[6:7], 1, v134
	v_ashrrev_i32_e32 v209, 31, v208
	s_waitcnt vmcnt(1)
	v_add_f32_e32 v114, v114, v115
	v_add_f32_e32 v115, v116, v117
	s_waitcnt vmcnt(0)
	v_add_f32_e32 v116, v128, v129
	v_add_f32_e32 v117, v130, v131
	v_add_f32_e32 v114, v114, v115
	v_add_f32_e32 v115, v116, v117
	v_add_f32_e32 v114, v114, v115
	v_fmamk_f32 v114, v114, 0x3b000000, v213
	v_mul_f32_e32 v115, 0x4f800000, v114
	v_cmp_gt_f32_e32 vcc, s90, v114
	s_nop 1
	v_cndmask_b32_e32 v115, v114, v115, vcc
	v_sqrt_f32_e32 v116, v115
	v_add_f32_e32 v114, v132, v133
	v_add_f32_e32 v114, v118, v114
	v_add_u32_e32 v117, -1, v116
	v_add_u32_e32 v118, 1, v116
	v_fma_f32 v119, -v117, v116, v115
	v_fma_f32 v128, -v118, v116, v115
	v_cmp_ge_f32_e64 s[8:9], 0, v119
	s_nop 1
	v_cndmask_b32_e64 v116, v116, v117, s[8:9]
	v_cmp_lt_f32_e64 s[8:9], 0, v128
	s_nop 1
	v_cndmask_b32_e64 v116, v116, v118, s[8:9]
	v_mul_f32_e32 v117, 0x37800000, v116
	v_cndmask_b32_e32 v116, v116, v117, vcc
	v_cmp_class_f32_e32 vcc, v115, v215
	s_nop 1
	v_cndmask_b32_e32 v115, v116, v115, vcc
	v_div_scale_f32 v116, s[8:9], v115, v115, 1.0
	v_rcp_f32_e32 v117, v116
	v_div_scale_f32 v118, vcc, 1.0, v115, 1.0
	s_and_b64 s[8:9], exec, s[62:63]
	v_fma_f32 v119, -v116, v117, 1.0
	v_fmac_f32_e32 v117, v119, v117
	v_mul_f32_e32 v119, v118, v117
	v_fma_f32 v128, -v116, v119, v118
	v_fmac_f32_e32 v119, v128, v117
	v_fma_f32 v116, -v116, v119, v118
	v_div_fmas_f32 v116, v116, v117, v119
	v_div_fixup_f32 v236, v116, v115, 1.0
	v_mul_f32_e32 v115, v236, v236
	s_mov_b64 vcc, s[8:9]
	s_cbranch_vccz .LBB0_404
	s_and_b64 vcc, exec, s[6:7]
	v_mul_f32_e32 v113, v114, v115
	s_cbranch_vccnz .LBB0_403
	v_mov_b64_e32 v[116:117], s[50:51]
	v_mad_i64_i32 v[116:117], s[8:9], v232, s65, v[116:117]
	v_lshl_add_u64 v[116:117], v[208:209], 1, v[116:117]
	global_load_dwordx2 v[160:161], v[116:117], off offset:2080
	global_load_dwordx2 v[162:163], v[116:117], off offset:2048
	v_add_u32_e32 v118, 0x10, v232
	v_mov_b64_e32 v[116:117], s[50:51]
	v_mad_i64_i32 v[116:117], s[8:9], v118, s65, v[116:117]
	v_lshl_add_u64 v[116:117], v[208:209], 1, v[116:117]
	global_load_dwordx2 v[164:165], v[116:117], off offset:2080
	global_load_dwordx2 v[166:167], v[116:117], off offset:2048
	v_add_u32_e32 v118, 0x20, v232
	v_mov_b64_e32 v[116:117], s[50:51]
	v_mad_i64_i32 v[116:117], s[8:9], v118, s65, v[116:117]
	v_lshl_add_u64 v[116:117], v[208:209], 1, v[116:117]
	global_load_dwordx2 v[168:169], v[116:117], off offset:2080
	global_load_dwordx2 v[170:171], v[116:117], off offset:2048
	v_add_u32_e32 v118, 0x30, v232
	v_mov_b64_e32 v[116:117], s[50:51]
	v_mad_i64_i32 v[116:117], s[8:9], v118, s65, v[116:117]
	v_lshl_add_u64 v[116:117], v[208:209], 1, v[116:117]
	global_load_dwordx2 v[172:173], v[116:117], off offset:2080
	global_load_dwordx2 v[174:175], v[116:117], off offset:2048
	v_add_u32_e32 v118, 0x80, v232
	v_mov_b64_e32 v[116:117], s[50:51]
	v_mad_i64_i32 v[116:117], s[8:9], v118, s65, v[116:117]
	v_lshl_add_u64 v[116:117], v[208:209], 1, v[116:117]
	global_load_dwordx2 v[176:177], v[116:117], off offset:2080
	global_load_dwordx2 v[178:179], v[116:117], off offset:2048
	v_add_u32_e32 v118, 0x90, v232
	v_mov_b64_e32 v[116:117], s[50:51]
	v_mad_i64_i32 v[116:117], s[8:9], v118, s65, v[116:117]
	v_lshl_add_u64 v[116:117], v[208:209], 1, v[116:117]
	global_load_dwordx2 v[180:181], v[116:117], off offset:2080
	global_load_dwordx2 v[182:183], v[116:117], off offset:2048
	v_add_u32_e32 v118, 0xa0, v232
	v_mov_b64_e32 v[116:117], s[50:51]
	v_mad_i64_i32 v[116:117], s[8:9], v118, s65, v[116:117]
	v_lshl_add_u64 v[116:117], v[208:209], 1, v[116:117]
	global_load_dwordx2 v[184:185], v[116:117], off offset:2080
	global_load_dwordx2 v[186:187], v[116:117], off offset:2048
	v_add_u32_e32 v118, 0xb0, v232
	v_mov_b64_e32 v[116:117], s[50:51]
	v_mad_i64_i32 v[116:117], s[8:9], v118, s65, v[116:117]
	v_lshl_add_u64 v[116:117], v[208:209], 1, v[116:117]
	global_load_dwordx2 v[188:189], v[116:117], off offset:2080
	global_load_dwordx2 v[190:191], v[116:117], off offset:2048
	s_waitcnt vmcnt(14)
	v_lshlrev_b32_e32 v129, 16, v160
	v_and_b32_e32 v131, 0xffff0000, v160
	v_and_b32_e32 v130, 0xffff0000, v162
	v_lshlrev_b32_e32 v133, 16, v161
	v_and_b32_e32 v119, 0xffff0000, v161
	v_and_b32_e32 v118, 0xffff0000, v163
	v_lshlrev_b32_e32 v128, 16, v162
	v_lshlrev_b32_e32 v132, 16, v163
	v_pk_mul_f32 v[116:117], v[130:131], v[130:131]
	v_pk_mul_f32 v[118:119], v[118:119], v[118:119]
	v_pk_fma_f32 v[116:117], v[128:129], v[128:129], v[116:117]
	v_pk_fma_f32 v[118:119], v[132:133], v[132:133], v[118:119]
	s_nop 0
	v_pk_add_f32 v[116:117], v[116:117], v[118:119]
	s_nop 0
	v_add_f32_e32 v113, v113, v116
	v_add_f32_e32 v113, v113, v117

.LBB0_410:
	s_or_b64 exec, exec, s[8:9]
	v_or_b32_e32 v238, 16, v232
	v_ashrrev_i32_e32 v239, 31, v238
	v_lshlrev_b64 v[112:113], 6, v[238:239]
	v_lshl_add_u64 v[112:113], s[16:17], 0, v[112:113]
	global_load_dwordx4 v[128:131], v[112:113], off
	global_load_dwordx4 v[132:135], v[112:113], off offset:16
	v_mul_f32_e32 v112, v109, v109
	v_mul_f32_e32 v113, v111, v111
	s_waitcnt lgkmcnt(0)
	v_mul_f32_e32 v117, v105, v105
	v_mul_f32_e32 v118, v107, v107
	v_fmac_f32_e32 v112, v108, v108
	v_fmac_f32_e32 v113, v110, v110
	v_fmac_f32_e32 v117, v104, v104
	v_fmac_f32_e32 v118, v106, v106
	v_cndmask_b32_e64 v119, 0, 1, s[62:63]
	v_add_f32_e32 v112, v112, v113
	v_add_f32_e32 v113, v117, v118
	v_cmp_ne_u32_e64 s[8:9], 1, v119
	v_add_f32_e32 v112, v112, v113
	s_mov_b64 s[26:27], -1
	s_waitcnt vmcnt(1)
	v_add_f32_e32 v128, v128, v129
	v_add_f32_e32 v129, v130, v131
	s_waitcnt vmcnt(0)
	v_add_f32_e32 v130, v132, v133
	v_add_f32_e32 v131, v134, v135
	v_add_f32_e32 v128, v128, v129
	v_add_f32_e32 v129, v130, v131
	v_add_f32_e32 v128, v128, v129
	v_fmamk_f32 v128, v128, 0x3b000000, v213
	v_mul_f32_e32 v129, 0x4f800000, v128
	v_cmp_gt_f32_e32 vcc, s90, v128
	s_nop 1
	v_cndmask_b32_e32 v128, v128, v129, vcc
	v_sqrt_f32_e32 v129, v128
	s_nop 0
	v_add_u32_e32 v117, -1, v129
	v_add_u32_e32 v118, 1, v129
	v_fma_f32 v119, -v117, v129, v128
	v_fma_f32 v130, -v118, v129, v128
	v_cmp_ge_f32_e64 s[14:15], 0, v119
	s_nop 1
	v_cndmask_b32_e64 v117, v129, v117, s[14:15]
	v_cmp_lt_f32_e64 s[14:15], 0, v130
	s_nop 1
	v_cndmask_b32_e64 v117, v117, v118, s[14:15]
	v_mul_f32_e32 v118, 0x37800000, v117
	v_cndmask_b32_e32 v117, v117, v118, vcc
	v_cmp_class_f32_e32 vcc, v128, v215
	s_nop 1
	v_cndmask_b32_e32 v117, v117, v128, vcc
	v_div_scale_f32 v118, s[14:15], v117, v117, 1.0
	v_rcp_f32_e32 v119, v118
	v_div_scale_f32 v113, vcc, 1.0, v117, 1.0
	v_fma_f32 v128, -v118, v119, 1.0
	v_fmac_f32_e32 v119, v128, v119
	v_mul_f32_e32 v128, v113, v119
	v_fma_f32 v129, -v118, v128, v113
	v_fmac_f32_e32 v128, v129, v119
	v_fma_f32 v113, -v118, v128, v113
	v_div_fmas_f32 v113, v113, v119, v128
	v_div_fixup_f32 v132, v113, v117, 1.0
	s_andn2_b64 vcc, exec, s[62:63]
	v_mul_f32_e32 v113, v132, v132
	s_cbranch_vccnz .LBB0_414
	s_and_b64 vcc, exec, s[6:7]
	v_mul_f32_e32 v117, v112, v113
	s_cbranch_vccnz .LBB0_413
	v_lshlrev_b32_e32 v131, 16, v164
	v_and_b32_e32 v135, 0xffff0000, v164
	v_and_b32_e32 v134, 0xffff0000, v166
	v_lshlrev_b32_e32 v137, 16, v165
	v_and_b32_e32 v129, 0xffff0000, v165
	v_and_b32_e32 v128, 0xffff0000, v167
	v_lshlrev_b32_e32 v130, 16, v166
	v_lshlrev_b32_e32 v136, 16, v167
	v_pk_mul_f32 v[118:119], v[134:135], v[134:135]
	v_pk_mul_f32 v[128:129], v[128:129], v[128:129]
	v_pk_fma_f32 v[118:119], v[130:131], v[130:131], v[118:119]
	v_pk_fma_f32 v[128:129], v[136:137], v[136:137], v[128:129]
	s_nop 0
	v_pk_add_f32 v[118:119], v[118:119], v[128:129]
	s_nop 0
	v_add_f32_e32 v117, v117, v118
	v_add_f32_e32 v117, v117, v119

.LBB0_420:
	s_or_b64 exec, exec, s[14:15]
	v_or_b32_e32 v228, 32, v232
	v_ashrrev_i32_e32 v229, 31, v228
	s_waitcnt lgkmcnt(0)
	v_lshlrev_b64 v[112:113], 6, v[228:229]
	v_lshl_add_u64 v[112:113], s[16:17], 0, v[112:113]
	global_load_dwordx4 v[128:131], v[112:113], off
	global_load_dwordx4 v[134:137], v[112:113], off offset:16
	v_mul_f32_e32 v112, v93, v93
	v_mul_f32_e32 v113, v95, v95
	v_mul_f32_e32 v117, v89, v89
	v_mul_f32_e32 v118, v91, v91
	v_fmac_f32_e32 v112, v92, v92
	v_fmac_f32_e32 v113, v94, v94
	v_fmac_f32_e32 v117, v88, v88
	v_fmac_f32_e32 v118, v90, v90
	v_add_f32_e32 v112, v112, v113
	v_add_f32_e32 v113, v117, v118
	v_add_f32_e32 v112, v112, v113
	s_mov_b64 s[26:27], -1
	s_waitcnt vmcnt(1)
	v_add_f32_e32 v119, v128, v129
	v_add_f32_e32 v128, v130, v131
	s_waitcnt vmcnt(0)
	v_add_f32_e32 v129, v134, v135
	v_add_f32_e32 v130, v136, v137
	v_add_f32_e32 v119, v119, v128
	v_add_f32_e32 v128, v129, v130
	v_add_f32_e32 v119, v119, v128
	v_fmamk_f32 v119, v119, 0x3b000000, v213
	v_mul_f32_e32 v128, 0x4f800000, v119
	v_cmp_gt_f32_e32 vcc, s90, v119
	s_nop 1
	v_cndmask_b32_e32 v119, v119, v128, vcc
	v_sqrt_f32_e32 v128, v119
	s_nop 0
	v_add_u32_e32 v117, -1, v128
	v_add_u32_e32 v118, 1, v128
	v_fma_f32 v129, -v117, v128, v119
	v_fma_f32 v130, -v118, v128, v119
	v_cmp_ge_f32_e64 s[14:15], 0, v129
	s_nop 1
	v_cndmask_b32_e64 v117, v128, v117, s[14:15]
	v_cmp_lt_f32_e64 s[14:15], 0, v130
	s_nop 1
	v_cndmask_b32_e64 v117, v117, v118, s[14:15]
	v_mul_f32_e32 v118, 0x37800000, v117
	v_cndmask_b32_e32 v117, v117, v118, vcc
	v_cmp_class_f32_e32 vcc, v119, v215
	s_nop 1
	v_cndmask_b32_e32 v117, v117, v119, vcc
	v_div_scale_f32 v118, s[14:15], v117, v117, 1.0
	v_rcp_f32_e32 v119, v118
	v_div_scale_f32 v113, vcc, 1.0, v117, 1.0
	v_fma_f32 v128, -v118, v119, 1.0
	v_fmac_f32_e32 v119, v128, v119
	v_mul_f32_e32 v128, v113, v119
	v_fma_f32 v129, -v118, v128, v113
	v_fmac_f32_e32 v128, v129, v119
	v_fma_f32 v113, -v118, v128, v113
	v_div_fmas_f32 v113, v113, v119, v128
	v_div_fixup_f32 v230, v113, v117, 1.0
	s_and_b64 vcc, exec, s[8:9]
	v_mul_f32_e32 v113, v230, v230
	s_cbranch_vccnz .LBB0_424
	s_and_b64 vcc, exec, s[6:7]
	v_mul_f32_e32 v117, v112, v113
	s_cbranch_vccnz .LBB0_423
	v_lshlrev_b32_e32 v131, 16, v168
	v_and_b32_e32 v135, 0xffff0000, v168
	v_and_b32_e32 v134, 0xffff0000, v170
	v_lshlrev_b32_e32 v137, 16, v169
	v_and_b32_e32 v129, 0xffff0000, v169
	v_and_b32_e32 v128, 0xffff0000, v171
	v_lshlrev_b32_e32 v130, 16, v170
	v_lshlrev_b32_e32 v136, 16, v171
	v_pk_mul_f32 v[118:119], v[134:135], v[134:135]
	v_pk_mul_f32 v[128:129], v[128:129], v[128:129]
	v_pk_fma_f32 v[118:119], v[130:131], v[130:131], v[118:119]
	v_pk_fma_f32 v[128:129], v[136:137], v[136:137], v[128:129]
	s_nop 0
	v_pk_add_f32 v[118:119], v[118:119], v[128:129]
	s_nop 0
	v_add_f32_e32 v117, v117, v118
	v_add_f32_e32 v117, v117, v119

.LBB0_430:
	s_or_b64 exec, exec, s[14:15]
	v_or_b32_e32 v234, 48, v232
	v_ashrrev_i32_e32 v235, 31, v234
	s_waitcnt lgkmcnt(0)
	v_lshlrev_b64 v[112:113], 6, v[234:235]
	v_lshl_add_u64 v[112:113], s[16:17], 0, v[112:113]
	global_load_dwordx4 v[128:131], v[112:113], off
	global_load_dwordx4 v[134:137], v[112:113], off offset:16
	v_mul_f32_e32 v112, v77, v77
	v_mul_f32_e32 v113, v79, v79
	v_mul_f32_e32 v117, v73, v73
	v_mul_f32_e32 v118, v75, v75
	v_fmac_f32_e32 v112, v76, v76
	v_fmac_f32_e32 v113, v78, v78
	v_fmac_f32_e32 v117, v72, v72
	v_fmac_f32_e32 v118, v74, v74
	v_add_f32_e32 v112, v112, v113
	v_add_f32_e32 v113, v117, v118
	v_add_f32_e32 v112, v112, v113
	s_mov_b64 s[26:27], -1
	s_waitcnt vmcnt(1)
	v_add_f32_e32 v119, v128, v129
	v_add_f32_e32 v128, v130, v131
	s_waitcnt vmcnt(0)
	v_add_f32_e32 v129, v134, v135
	v_add_f32_e32 v130, v136, v137
	v_add_f32_e32 v119, v119, v128
	v_add_f32_e32 v128, v129, v130
	v_add_f32_e32 v119, v119, v128
	v_fmamk_f32 v119, v119, 0x3b000000, v213
	v_mul_f32_e32 v128, 0x4f800000, v119
	v_cmp_gt_f32_e32 vcc, s90, v119
	s_nop 1
	v_cndmask_b32_e32 v119, v119, v128, vcc
	v_sqrt_f32_e32 v128, v119
	s_nop 0
	v_add_u32_e32 v117, -1, v128
	v_add_u32_e32 v118, 1, v128
	v_fma_f32 v129, -v117, v128, v119
	v_fma_f32 v130, -v118, v128, v119
	v_cmp_ge_f32_e64 s[14:15], 0, v129
	s_nop 1
	v_cndmask_b32_e64 v117, v128, v117, s[14:15]
	v_cmp_lt_f32_e64 s[14:15], 0, v130
	s_nop 1
	v_cndmask_b32_e64 v117, v117, v118, s[14:15]
	v_mul_f32_e32 v118, 0x37800000, v117
	v_cndmask_b32_e32 v117, v117, v118, vcc
	v_cmp_class_f32_e32 vcc, v119, v215
	s_nop 1
	v_cndmask_b32_e32 v117, v117, v119, vcc
	v_div_scale_f32 v118, s[14:15], v117, v117, 1.0
	v_rcp_f32_e32 v119, v118
	v_div_scale_f32 v113, vcc, 1.0, v117, 1.0
	v_fma_f32 v128, -v118, v119, 1.0
	v_fmac_f32_e32 v119, v128, v119
	v_mul_f32_e32 v128, v113, v119
	v_fma_f32 v129, -v118, v128, v113
	v_fmac_f32_e32 v128, v129, v119
	v_fma_f32 v113, -v118, v128, v113
	v_div_fmas_f32 v113, v113, v119, v128
	v_div_fixup_f32 v226, v113, v117, 1.0
	s_and_b64 vcc, exec, s[8:9]
	v_mul_f32_e32 v113, v226, v226
	s_cbranch_vccnz .LBB0_434
	s_and_b64 vcc, exec, s[6:7]
	v_mul_f32_e32 v117, v112, v113
	s_cbranch_vccnz .LBB0_433
	v_lshlrev_b32_e32 v131, 16, v172
	v_and_b32_e32 v135, 0xffff0000, v172
	v_and_b32_e32 v134, 0xffff0000, v174
	v_lshlrev_b32_e32 v137, 16, v173
	v_and_b32_e32 v129, 0xffff0000, v173
	v_and_b32_e32 v128, 0xffff0000, v175
	v_lshlrev_b32_e32 v130, 16, v174
	v_lshlrev_b32_e32 v136, 16, v175
	v_pk_mul_f32 v[118:119], v[134:135], v[134:135]
	v_pk_mul_f32 v[128:129], v[128:129], v[128:129]
	v_pk_fma_f32 v[118:119], v[130:131], v[130:131], v[118:119]
	v_pk_fma_f32 v[128:129], v[136:137], v[136:137], v[128:129]
	s_nop 0
	v_pk_add_f32 v[118:119], v[118:119], v[128:129]
	s_nop 0
	v_add_f32_e32 v117, v117, v118
	v_add_f32_e32 v117, v117, v119

.LBB0_440:
	s_or_b64 exec, exec, s[14:15]
	v_add_u32_e32 v112, 0x80, v232
	s_waitcnt lgkmcnt(0)
	v_ashrrev_i32_e32 v113, 31, v112
	v_lshlrev_b64 v[118:119], 6, v[112:113]
	v_lshl_add_u64 v[118:119], s[16:17], 0, v[118:119]
	global_load_dwordx4 v[128:131], v[118:119], off
	global_load_dwordx4 v[134:137], v[118:119], off offset:16
	v_mul_f32_e32 v113, v61, v61
	v_mul_f32_e32 v117, v63, v63
	v_mul_f32_e32 v118, v57, v57
	v_mul_f32_e32 v119, v59, v59
	v_fmac_f32_e32 v113, v60, v60
	v_fmac_f32_e32 v117, v62, v62
	v_fmac_f32_e32 v118, v56, v56
	v_fmac_f32_e32 v119, v58, v58
	v_add_f32_e32 v113, v113, v117
	v_add_f32_e32 v117, v118, v119
	v_add_f32_e32 v113, v113, v117
	s_mov_b64 s[26:27], -1
	s_waitcnt vmcnt(1)
	v_add_f32_e32 v128, v128, v129
	v_add_f32_e32 v129, v130, v131
	s_waitcnt vmcnt(0)
	v_add_f32_e32 v130, v134, v135
	v_add_f32_e32 v131, v136, v137
	v_add_f32_e32 v128, v128, v129
	v_add_f32_e32 v129, v130, v131
	v_add_f32_e32 v128, v128, v129
	v_fmamk_f32 v128, v128, 0x3b000000, v213
	v_mul_f32_e32 v129, 0x4f800000, v128
	v_cmp_gt_f32_e32 vcc, s90, v128
	s_nop 1
	v_cndmask_b32_e32 v128, v128, v129, vcc
	v_sqrt_f32_e32 v129, v128
	s_nop 0
	v_add_u32_e32 v118, -1, v129
	v_add_u32_e32 v119, 1, v129
	v_fma_f32 v130, -v118, v129, v128
	v_fma_f32 v131, -v119, v129, v128
	v_cmp_ge_f32_e64 s[14:15], 0, v130
	s_nop 1
	v_cndmask_b32_e64 v118, v129, v118, s[14:15]
	v_cmp_lt_f32_e64 s[14:15], 0, v131
	s_nop 1
	v_cndmask_b32_e64 v118, v118, v119, s[14:15]
	v_mul_f32_e32 v119, 0x37800000, v118
	v_cndmask_b32_e32 v118, v118, v119, vcc
	v_cmp_class_f32_e32 vcc, v128, v215
	s_nop 1
	v_cndmask_b32_e32 v118, v118, v128, vcc
	v_div_scale_f32 v119, s[14:15], v118, v118, 1.0
	v_rcp_f32_e32 v128, v119
	v_div_scale_f32 v117, vcc, 1.0, v118, 1.0
	v_fma_f32 v129, -v119, v128, 1.0
	v_fmac_f32_e32 v128, v129, v128
	v_mul_f32_e32 v129, v117, v128
	v_fma_f32 v130, -v119, v129, v117
	v_fmac_f32_e32 v129, v130, v128
	v_fma_f32 v117, -v119, v129, v117
	v_div_fmas_f32 v117, v117, v128, v129
	v_div_fixup_f32 v220, v117, v118, 1.0
	s_and_b64 vcc, exec, s[8:9]
	v_mul_f32_e32 v117, v220, v220
	s_cbranch_vccnz .LBB0_444
	s_and_b64 vcc, exec, s[6:7]
	v_mul_f32_e32 v118, v113, v117
	s_cbranch_vccnz .LBB0_443
	v_lshlrev_b32_e32 v135, 16, v176
	v_and_b32_e32 v137, 0xffff0000, v176
	v_and_b32_e32 v136, 0xffff0000, v178
	v_lshlrev_b32_e32 v139, 16, v177
	v_and_b32_e32 v131, 0xffff0000, v177
	v_and_b32_e32 v130, 0xffff0000, v179
	v_lshlrev_b32_e32 v134, 16, v178
	v_lshlrev_b32_e32 v138, 16, v179
	v_pk_mul_f32 v[128:129], v[136:137], v[136:137]
	v_pk_mul_f32 v[130:131], v[130:131], v[130:131]
	v_pk_fma_f32 v[128:129], v[134:135], v[134:135], v[128:129]
	v_pk_fma_f32 v[130:131], v[138:139], v[138:139], v[130:131]
	s_nop 0
	v_pk_add_f32 v[128:129], v[128:129], v[130:131]
	s_nop 0
	v_add_f32_e32 v112, v118, v128
	v_add_f32_e32 v118, v112, v129

.LBB0_450:
	s_or_b64 exec, exec, s[14:15]
	v_add_u32_e32 v112, 0x90, v232
	s_waitcnt lgkmcnt(0)
	v_ashrrev_i32_e32 v113, 31, v112
	v_lshlrev_b64 v[118:119], 6, v[112:113]
	v_lshl_add_u64 v[118:119], s[16:17], 0, v[118:119]
	global_load_dwordx4 v[128:131], v[118:119], off
	global_load_dwordx4 v[134:137], v[118:119], off offset:16
	v_mul_f32_e32 v113, v45, v45
	v_mul_f32_e32 v117, v47, v47
	v_mul_f32_e32 v118, v41, v41
	v_mul_f32_e32 v119, v43, v43
	v_fmac_f32_e32 v113, v44, v44
	v_fmac_f32_e32 v117, v46, v46
	v_fmac_f32_e32 v118, v40, v40
	v_fmac_f32_e32 v119, v42, v42
	v_add_f32_e32 v113, v113, v117
	v_add_f32_e32 v117, v118, v119
	v_add_f32_e32 v113, v113, v117
	s_mov_b64 s[26:27], -1
	s_waitcnt vmcnt(1)
	v_add_f32_e32 v128, v128, v129
	v_add_f32_e32 v129, v130, v131
	s_waitcnt vmcnt(0)
	v_add_f32_e32 v130, v134, v135
	v_add_f32_e32 v131, v136, v137
	v_add_f32_e32 v128, v128, v129
	v_add_f32_e32 v129, v130, v131
	v_add_f32_e32 v128, v128, v129
	v_fmamk_f32 v128, v128, 0x3b000000, v213
	v_mul_f32_e32 v129, 0x4f800000, v128
	v_cmp_gt_f32_e32 vcc, s90, v128
	s_nop 1
	v_cndmask_b32_e32 v128, v128, v129, vcc
	v_sqrt_f32_e32 v129, v128
	s_nop 0
	v_add_u32_e32 v118, -1, v129
	v_add_u32_e32 v119, 1, v129
	v_fma_f32 v130, -v118, v129, v128
	v_fma_f32 v131, -v119, v129, v128
	v_cmp_ge_f32_e64 s[14:15], 0, v130
	s_nop 1
	v_cndmask_b32_e64 v118, v129, v118, s[14:15]
	v_cmp_lt_f32_e64 s[14:15], 0, v131
	s_nop 1
	v_cndmask_b32_e64 v118, v118, v119, s[14:15]
	v_mul_f32_e32 v119, 0x37800000, v118
	v_cndmask_b32_e32 v118, v118, v119, vcc
	v_cmp_class_f32_e32 vcc, v128, v215
	s_nop 1
	v_cndmask_b32_e32 v118, v118, v128, vcc
	v_div_scale_f32 v119, s[14:15], v118, v118, 1.0
	v_rcp_f32_e32 v128, v119
	v_div_scale_f32 v117, vcc, 1.0, v118, 1.0
	v_fma_f32 v129, -v119, v128, 1.0
	v_fmac_f32_e32 v128, v129, v128
	v_mul_f32_e32 v129, v117, v128
	v_fma_f32 v130, -v119, v129, v117
	v_fmac_f32_e32 v129, v130, v128
	v_fma_f32 v117, -v119, v129, v117
	v_div_fmas_f32 v117, v117, v128, v129
	v_div_fixup_f32 v214, v117, v118, 1.0
	s_and_b64 vcc, exec, s[8:9]
	v_mul_f32_e32 v117, v214, v214
	s_cbranch_vccnz .LBB0_454
	s_and_b64 vcc, exec, s[6:7]
	v_mul_f32_e32 v118, v113, v117
	s_cbranch_vccnz .LBB0_453
	v_lshlrev_b32_e32 v135, 16, v180
	v_and_b32_e32 v137, 0xffff0000, v180
	v_and_b32_e32 v136, 0xffff0000, v182
	v_lshlrev_b32_e32 v139, 16, v181
	v_and_b32_e32 v131, 0xffff0000, v181
	v_and_b32_e32 v130, 0xffff0000, v183
	v_lshlrev_b32_e32 v134, 16, v182
	v_lshlrev_b32_e32 v138, 16, v183
	v_pk_mul_f32 v[128:129], v[136:137], v[136:137]
	v_pk_mul_f32 v[130:131], v[130:131], v[130:131]
	v_pk_fma_f32 v[128:129], v[134:135], v[134:135], v[128:129]
	v_pk_fma_f32 v[130:131], v[138:139], v[138:139], v[130:131]
	s_nop 0
	v_pk_add_f32 v[128:129], v[128:129], v[130:131]
	s_nop 0
	v_add_f32_e32 v112, v118, v128
	v_add_f32_e32 v118, v112, v129

.LBB0_460:
	s_or_b64 exec, exec, s[14:15]
	v_add_u32_e32 v112, 0xa0, v232
	s_waitcnt lgkmcnt(0)
	v_ashrrev_i32_e32 v113, 31, v112
	v_lshlrev_b64 v[118:119], 6, v[112:113]
	v_lshl_add_u64 v[118:119], s[16:17], 0, v[118:119]
	global_load_dwordx4 v[128:131], v[118:119], off
	global_load_dwordx4 v[134:137], v[118:119], off offset:16
	v_mul_f32_e32 v113, v29, v29
	v_mul_f32_e32 v117, v31, v31
	v_mul_f32_e32 v118, v25, v25
	v_mul_f32_e32 v119, v27, v27
	v_fmac_f32_e32 v113, v28, v28
	v_fmac_f32_e32 v117, v30, v30
	v_fmac_f32_e32 v118, v24, v24
	v_fmac_f32_e32 v119, v26, v26
	v_add_f32_e32 v113, v113, v117
	v_add_f32_e32 v117, v118, v119
	v_add_f32_e32 v113, v113, v117
	s_mov_b64 s[26:27], -1
	s_waitcnt vmcnt(1)
	v_add_f32_e32 v128, v128, v129
	v_add_f32_e32 v129, v130, v131
	s_waitcnt vmcnt(0)
	v_add_f32_e32 v130, v134, v135
	v_add_f32_e32 v131, v136, v137
	v_add_f32_e32 v128, v128, v129
	v_add_f32_e32 v129, v130, v131
	v_add_f32_e32 v128, v128, v129
	v_fmamk_f32 v128, v128, 0x3b000000, v213
	v_mul_f32_e32 v129, 0x4f800000, v128
	v_cmp_gt_f32_e32 vcc, s90, v128
	s_nop 1
	v_cndmask_b32_e32 v128, v128, v129, vcc
	v_sqrt_f32_e32 v129, v128
	s_nop 0
	v_add_u32_e32 v118, -1, v129
	v_add_u32_e32 v119, 1, v129
	v_fma_f32 v130, -v118, v129, v128
	v_fma_f32 v131, -v119, v129, v128
	v_cmp_ge_f32_e64 s[14:15], 0, v130
	s_nop 1
	v_cndmask_b32_e64 v118, v129, v118, s[14:15]
	v_cmp_lt_f32_e64 s[14:15], 0, v131
	s_nop 1
	v_cndmask_b32_e64 v118, v118, v119, s[14:15]
	v_mul_f32_e32 v119, 0x37800000, v118
	v_cndmask_b32_e32 v118, v118, v119, vcc
	v_cmp_class_f32_e32 vcc, v128, v215
	s_nop 1
	v_cndmask_b32_e32 v118, v118, v128, vcc
	v_div_scale_f32 v119, s[14:15], v118, v118, 1.0
	v_rcp_f32_e32 v128, v119
	v_div_scale_f32 v117, vcc, 1.0, v118, 1.0
	v_fma_f32 v129, -v119, v128, 1.0
	v_fmac_f32_e32 v128, v129, v128
	v_mul_f32_e32 v129, v117, v128
	v_fma_f32 v130, -v119, v129, v117
	v_fmac_f32_e32 v129, v130, v128
	v_fma_f32 v117, -v119, v129, v117
	v_div_fmas_f32 v117, v117, v128, v129
	v_div_fixup_f32 v212, v117, v118, 1.0
	s_and_b64 vcc, exec, s[8:9]
	v_mul_f32_e32 v117, v212, v212
	s_cbranch_vccnz .LBB0_464
	s_and_b64 vcc, exec, s[6:7]
	v_mul_f32_e32 v118, v113, v117
	s_cbranch_vccnz .LBB0_463
	v_lshlrev_b32_e32 v135, 16, v184
	v_and_b32_e32 v137, 0xffff0000, v184
	v_and_b32_e32 v136, 0xffff0000, v186
	v_lshlrev_b32_e32 v139, 16, v185
	v_and_b32_e32 v131, 0xffff0000, v185
	v_and_b32_e32 v130, 0xffff0000, v187
	v_lshlrev_b32_e32 v134, 16, v186
	v_lshlrev_b32_e32 v138, 16, v187
	v_pk_mul_f32 v[128:129], v[136:137], v[136:137]
	v_pk_mul_f32 v[130:131], v[130:131], v[130:131]
	v_pk_fma_f32 v[128:129], v[134:135], v[134:135], v[128:129]
	v_pk_fma_f32 v[130:131], v[138:139], v[138:139], v[130:131]
	s_nop 0
	v_pk_add_f32 v[128:129], v[128:129], v[130:131]
	s_nop 0
	v_add_f32_e32 v112, v118, v128
	v_add_f32_e32 v118, v112, v129

.LBB0_470:
	s_or_b64 exec, exec, s[14:15]
	v_add_u32_e32 v112, 0xb0, v232
	s_waitcnt lgkmcnt(0)
	v_ashrrev_i32_e32 v113, 31, v112
	v_lshlrev_b64 v[116:117], 6, v[112:113]
	v_lshl_add_u64 v[128:129], s[16:17], 0, v[116:117]
	global_load_dwordx4 v[116:119], v[128:129], off
	s_nop 0
	global_load_dwordx4 v[128:131], v[128:129], off offset:16
	v_mul_f32_e32 v113, v13, v13
	v_mul_f32_e32 v133, v15, v15
	v_mul_f32_e32 v134, v9, v9
	v_mul_f32_e32 v135, v11, v11
	v_fmac_f32_e32 v113, v12, v12
	v_fmac_f32_e32 v133, v14, v14
	v_fmac_f32_e32 v134, v8, v8
	v_fmac_f32_e32 v135, v10, v10
	v_add_f32_e32 v113, v113, v133
	s_mov_b64 s[14:15], -1
	s_waitcnt vmcnt(1)
	v_add_f32_e32 v116, v116, v117
	v_add_f32_e32 v117, v118, v119
	s_waitcnt vmcnt(0)
	v_add_f32_e32 v118, v128, v129
	v_add_f32_e32 v119, v130, v131
	v_add_f32_e32 v116, v116, v117
	v_add_f32_e32 v117, v118, v119
	v_add_f32_e32 v116, v116, v117
	v_fmamk_f32 v116, v116, 0x3b000000, v213
	v_mul_f32_e32 v117, 0x4f800000, v116
	v_cmp_gt_f32_e32 vcc, s90, v116
	v_add_f32_e32 v118, v134, v135
	v_add_f32_e32 v113, v113, v118
	v_cndmask_b32_e32 v116, v116, v117, vcc
	v_sqrt_f32_e32 v117, v116
	s_nop 0
	v_add_u32_e32 v119, -1, v117
	v_add_u32_e32 v128, 1, v117
	v_fma_f32 v129, -v119, v117, v116
	v_fma_f32 v130, -v128, v117, v116
	v_cmp_ge_f32_e64 s[12:13], 0, v129
	s_nop 1
	v_cndmask_b32_e64 v117, v117, v119, s[12:13]
	v_cmp_lt_f32_e64 s[12:13], 0, v130
	s_nop 1
	v_cndmask_b32_e64 v117, v117, v128, s[12:13]
	v_mul_f32_e32 v119, 0x37800000, v117
	v_cndmask_b32_e32 v117, v117, v119, vcc
	v_cmp_class_f32_e32 vcc, v116, v215
	s_nop 1
	v_cndmask_b32_e32 v116, v117, v116, vcc
	v_div_scale_f32 v117, s[12:13], v116, v116, 1.0
	v_rcp_f32_e32 v119, v117
	v_div_scale_f32 v118, vcc, 1.0, v116, 1.0
	v_fma_f32 v128, -v117, v119, 1.0
	v_fmac_f32_e32 v119, v128, v119
	v_mul_f32_e32 v128, v118, v119
	v_fma_f32 v129, -v117, v128, v118
	v_fmac_f32_e32 v128, v129, v119
	v_fma_f32 v117, -v117, v128, v118
	v_div_fmas_f32 v117, v117, v119, v128
	v_div_fixup_f32 v210, v117, v116, 1.0
	s_and_b64 vcc, exec, s[8:9]
	v_mul_f32_e32 v116, v210, v210
	s_cbranch_vccnz .LBB0_474
	s_and_b64 vcc, exec, s[6:7]
	v_mul_f32_e32 v117, v113, v116
	s_cbranch_vccnz .LBB0_473
	v_lshlrev_b32_e32 v131, 16, v188
	v_and_b32_e32 v135, 0xffff0000, v188
	v_and_b32_e32 v134, 0xffff0000, v190
	v_lshlrev_b32_e32 v137, 16, v189
	v_and_b32_e32 v129, 0xffff0000, v189
	v_and_b32_e32 v128, 0xffff0000, v191
	v_lshlrev_b32_e32 v130, 16, v190
	v_lshlrev_b32_e32 v136, 16, v191
	v_pk_mul_f32 v[118:119], v[134:135], v[134:135]
	v_pk_mul_f32 v[128:129], v[128:129], v[128:129]
	v_pk_fma_f32 v[118:119], v[130:131], v[130:131], v[118:119]
	v_pk_fma_f32 v[128:129], v[136:137], v[136:137], v[128:129]
	s_nop 0
	v_pk_add_f32 v[118:119], v[118:119], v[128:129]
	s_nop 0
	v_add_f32_e32 v112, v117, v118
	v_add_f32_e32 v117, v112, v119
